# adds P1 row loop: norm1_g hoisted, all scale/shift chunk loads issued at row top, next row x prefetched (double buffer)
# speedup vs baseline: 1.0073x; 1.0036x over previous
; __device__ __forceinline__ unsigned pk2(float lo, float hi) { return f2bf(lo) | (f2bf(hi) << 16); }
; __device__ __forceinline__ void p1_modulate(Frame& F, const Args& A) {
;     ...
;     for (int m = gw; m < T; m += NGW) {
;         const int b = m / SEQ; const float* xr = A.in[I_X] + (size_t)m * DM + 4 * F.lane; f32x4 v[8]; float s = 0.f;
; #pragma unroll
;         for (int j = 0; j < 8; ++j) { v[j] = *(const f32x4*)(xr + 256 * j); s += (v[j].x * v[j].x + v[j].y * v[j].y) + (v[j].z * v[j].z + v[j].w * v[j].w); }
;         const float rstd = 1.0f / sqrtf(wave_sum(s) * (1.0f / DM) + EPS);
;         bf16* ur = WSP(bf16, WS_U) + (size_t)m * DM + 4 * F.lane;
; #pragma unroll
;         for (int j = 0; j < 8; ++j) { const int k = 4 * F.lane + 256 * j;
;             const f32x4 g = *(const f32x4*)(A.in[I_N1G] + k), sc = *(const f32x4*)(MOD + b * 12288 + 1 * DM + k), sh = *(const f32x4*)(MOD + b * 12288 + k);
;             const f32x4 u = v[j] * rstd * g * (sc + 1.0f) + sh; if constexpr (NLB > 0) { v2u o; o.x = pk2(u.x, u.y); o.y = pk2(u.z, u.w); *(v2u*)(ur + 256 * j) = o; }
;             int w8 = __builtin_amdgcn_cvt_pk_fp8_f32(u.x, u.y, 0, false); w8 = __builtin_amdgcn_cvt_pk_fp8_f32(u.z, u.w, w8, true); *(int*)(WSP(unsigned char, WS_U8Q) + (size_t)m * DM + 4 * F.lane + 256 * j) = w8; }
.LBB0_53:
	s_lshl_b32 s0, s90, 3
	v_readlane_b32 s1, v246, 40
	s_add_i32 s42, s0, s1
	s_cmpk_gt_i32 s42, 0x1fff
	s_cbranch_scc1 .LBB0_56
	v_mbcnt_lo_u32_b32 v7, -1, 0
	v_mbcnt_hi_u32_b32 v7, -1, v7
	v_and_b32_e32 v9, 64, v7
	v_add_u32_e32 v9, 64, v9
	v_xor_b32_e32 v11, 1, v7
	v_cmp_lt_i32_e32 vcc, v11, v9
	v_readlane_b32 s48, v246, 3
	s_waitcnt lgkmcnt(0)
	v_lshlrev_b32_e32 v2, 2, v1
	v_cndmask_b32_e32 v11, v7, v11, vcc
	v_lshlrev_b32_e32 v48, 2, v11
	v_xor_b32_e32 v11, 2, v7
	v_cmp_lt_i32_e32 vcc, v11, v9
	v_readlane_b32 s49, v246, 4
	s_ashr_i32 s43, s42, 31
	v_cndmask_b32_e32 v11, v7, v11, vcc
	v_lshlrev_b32_e32 v49, 2, v11
	v_xor_b32_e32 v11, 4, v7
	v_cmp_lt_i32_e32 vcc, v11, v9
	s_lshl_b32 s44, s86, 3
	v_mov_b32_e32 v3, 0
	v_cndmask_b32_e32 v11, v7, v11, vcc
	v_lshlrev_b32_e32 v50, 2, v11
	v_xor_b32_e32 v11, 8, v7
	v_readlane_b32 s56, v246, 11
	v_readlane_b32 s57, v246, 12
	s_mov_b64 s[40:41], s[48:49]
	v_or_b32_e32 v12, 0x400, v2
	v_cmp_lt_i32_e32 vcc, v11, v9
	s_lshl_b64 s[0:1], s[42:43], 13
	s_mov_b64 s[48:49], s[56:57]
	v_lshlrev_b32_e32 v14, 2, v12
	v_mov_b32_e32 v15, v3
	v_cndmask_b32_e32 v11, v7, v11, vcc
	s_add_u32 s0, s40, s0
	v_lshlrev_b32_e32 v4, 4, v1
	v_mov_b32_e32 v5, v3
	v_lshl_add_u64 v[36:37], s[48:49], 0, v[14:15]
	v_or_b32_e32 v14, 0x500, v2
	v_lshlrev_b32_e32 v51, 2, v11
	v_xor_b32_e32 v11, 16, v7
	s_addc_u32 s1, s41, s1
	v_lshl_add_u64 v[34:35], s[48:49], 0, v[4:5]
	v_lshlrev_b32_e32 v16, 2, v14
	v_mov_b32_e32 v17, v3
	v_cmp_lt_i32_e32 vcc, v11, v9
	v_lshl_add_u64 v[4:5], s[0:1], 0, v[4:5]
	s_mov_b64 s[0:1], 0x1000
	s_ashr_i32 s45, s44, 31
	v_lshl_add_u64 v[38:39], s[48:49], 0, v[16:17]
	v_or_b32_e32 v16, 0x600, v2
	v_cndmask_b32_e32 v11, v7, v11, vcc
	v_lshl_add_u64 v[44:45], v[4:5], 0, s[0:1]
	s_lshl_b64 s[46:47], s[44:45], 13
	s_lshl_b64 s[0:1], s[42:43], 11
	v_lshlrev_b32_e32 v18, 2, v16
	v_mov_b32_e32 v19, v3
	v_lshlrev_b32_e32 v52, 2, v11
	v_xor_b32_e32 v11, 32, v7
	s_add_u32 s0, s30, s0
	v_lshl_add_u64 v[40:41], s[48:49], 0, v[18:19]
	v_or_b32_e32 v18, 0x700, v2
	v_cmp_lt_i32_e32 vcc, v11, v9
	s_addc_u32 s1, s31, s1
	v_readlane_b32 s54, v246, 9
	v_readlane_b32 s55, v246, 10
	v_or_b32_e32 v6, 0x100, v2
	v_or_b32_e32 v8, 0x200, v2
	v_or_b32_e32 v10, 0x300, v2
	v_lshlrev_b32_e32 v20, 2, v18
	v_mov_b32_e32 v21, v3
	v_cndmask_b32_e32 v7, v7, v11, vcc
	v_lshl_add_u64 v[4:5], s[0:1], 0, v[2:3]
	s_mov_b64 s[0:1], 0x30200000
	v_lshl_add_u64 v[42:43], s[48:49], 0, v[20:21]
	v_lshlrev_b32_e32 v53, 2, v7
	v_lshl_add_u64 v[46:47], v[4:5], 0, s[0:1]
	s_lshl_b64 s[54:55], s[44:45], 11
	v_mov_b32_e32 v54, 0x3727c5ac
	s_mov_b32 s0, 0xf800000
	v_mov_b32_e32 v55, 0x260
	v_lshlrev_b32_e32 v56, 2, v2
	v_lshlrev_b32_e32 v57, 2, v6
	v_lshlrev_b32_e32 v58, 2, v8
	v_lshlrev_b32_e32 v59, 2, v10
	v_lshlrev_b32_e32 v60, 2, v12
	v_lshlrev_b32_e32 v61, 2, v14
	v_lshlrev_b32_e32 v62, 2, v16
	v_lshlrev_b32_e32 v63, 2, v18
	v_readlane_b32 s50, v246, 5
	v_readlane_b32 s51, v246, 6
	v_readlane_b32 s52, v246, 7
	v_readlane_b32 s53, v246, 8
	v_readlane_b32 s58, v246, 13
	v_readlane_b32 s59, v246, 14
	v_readlane_b32 s60, v246, 15
	v_readlane_b32 s61, v246, 16
	v_readlane_b32 s62, v246, 17
	v_readlane_b32 s63, v246, 18
	global_load_dwordx4 v[176:179], v[44:45], off offset:-4096
	global_load_dwordx4 v[180:183], v[44:45], off offset:-3072
	global_load_dwordx4 v[184:187], v[44:45], off offset:-2048
	global_load_dwordx4 v[196:199], v[44:45], off offset:-1024
	global_load_dwordx4 v[236:239], v[44:45], off
	global_load_dwordx4 v[240:243], v[44:45], off offset:1024
	global_load_dwordx4 v[248:251], v[44:45], off offset:2048
	global_load_dwordx4 v[252:255], v[44:45], off offset:3072
	global_load_dwordx4 v[112:115], v[34:35], off
	global_load_dwordx4 v[116:119], v[34:35], off offset:1024
	global_load_dwordx4 v[120:123], v[34:35], off offset:2048
	global_load_dwordx4 v[124:127], v[34:35], off offset:3072
	global_load_dwordx4 v[128:131], v[36:37], off
	global_load_dwordx4 v[132:135], v[38:39], off
	global_load_dwordx4 v[136:139], v[40:41], off
	global_load_dwordx4 v[140:143], v[42:43], off
.LBB0_55:
	s_ashr_i32 s1, s42, 31
	s_lshr_b32 s1, s1, 20
	s_add_i32 s1, s42, s1
	s_lshr_b32 s1, s1, 12
	s_mul_i32 s2, s1, 0x3000
	s_ashr_i32 s3, s2, 31
	s_lshl_b64 s[2:3], s[2:3], 2
	s_add_u32 s56, s8, s2
	s_addc_u32 s57, s9, s3
	s_add_u32 s58, s56, 0x2000
	s_addc_u32 s59, s57, 0
	global_load_dwordx4 v[144:147], v56, s[58:59]
	global_load_dwordx4 v[148:151], v57, s[58:59]
	global_load_dwordx4 v[152:155], v58, s[58:59]
	global_load_dwordx4 v[156:159], v59, s[58:59]
	global_load_dwordx4 v[160:163], v60, s[58:59]
	global_load_dwordx4 v[164:167], v61, s[58:59]
	global_load_dwordx4 v[168:171], v62, s[58:59]
	global_load_dwordx4 v[172:175], v63, s[58:59]
	global_load_dwordx4 v[204:207], v56, s[56:57]
	global_load_dwordx4 v[208:211], v56, s[56:57] offset:1024
	global_load_dwordx4 v[212:215], v56, s[56:57] offset:2048
	global_load_dwordx4 v[216:219], v56, s[56:57] offset:3072
	global_load_dwordx4 v[220:223], v60, s[56:57]
	global_load_dwordx4 v[224:227], v61, s[56:57]
	global_load_dwordx4 v[228:231], v62, s[56:57]
	global_load_dwordx4 v[232:235], v63, s[56:57]
	s_add_i32 s42, s42, s44
	s_cmpk_lt_i32 s42, 0x2000
	s_cselect_b64 s[2:3], s[46:47], 0
	s_waitcnt vmcnt(24)
; __device__ __forceinline__ unsigned pk2(float lo, float hi) { return f2bf(lo) | (f2bf(hi) << 16); }
; __device__ __forceinline__ void p1_modulate(Frame& F, const Args& A) {
;     ...
;     for (int m = gw; m < T; m += NGW) {
;         const int b = m / SEQ; const float* xr = A.in[I_X] + (size_t)m * DM + 4 * F.lane; f32x4 v[8]; float s = 0.f;
; #pragma unroll
;         for (int j = 0; j < 8; ++j) { v[j] = *(const f32x4*)(xr + 256 * j); s += (v[j].x * v[j].x + v[j].y * v[j].y) + (v[j].z * v[j].z + v[j].w * v[j].w); }
;         const float rstd = 1.0f / sqrtf(wave_sum(s) * (1.0f / DM) + EPS);
;         bf16* ur = WSP(bf16, WS_U) + (size_t)m * DM + 4 * F.lane;
; #pragma unroll
;         for (int j = 0; j < 8; ++j) { const int k = 4 * F.lane + 256 * j;
;             const f32x4 g = *(const f32x4*)(A.in[I_N1G] + k), sc = *(const f32x4*)(MOD + b * 12288 + 1 * DM + k), sh = *(const f32x4*)(MOD + b * 12288 + k);
;             const f32x4 u = v[j] * rstd * g * (sc + 1.0f) + sh; if constexpr (NLB > 0) { v2u o; o.x = pk2(u.x, u.y); o.y = pk2(u.z, u.w); *(v2u*)(ur + 256 * j) = o; }
;             int w8 = __builtin_amdgcn_cvt_pk_fp8_f32(u.x, u.y, 0, false); w8 = __builtin_amdgcn_cvt_pk_fp8_f32(u.z, u.w, w8, true); *(int*)(WSP(unsigned char, WS_U8Q) + (size_t)m * DM + 4 * F.lane + 256 * j) = w8; }
	v_mov_b64_e32 v[30:31], v[176:177]
	v_mov_b64_e32 v[32:33], v[178:179]
	v_mov_b64_e32 v[22:23], v[180:181]
	v_mov_b64_e32 v[24:25], v[182:183]
	v_mov_b64_e32 v[18:19], v[184:185]
	v_mov_b64_e32 v[20:21], v[186:187]
	v_mov_b64_e32 v[26:27], v[196:197]
	v_mov_b64_e32 v[28:29], v[198:199]
	v_mov_b64_e32 v[14:15], v[236:237]
	v_mov_b64_e32 v[16:17], v[238:239]
	v_mov_b64_e32 v[10:11], v[240:241]
	v_mov_b64_e32 v[12:13], v[242:243]
	v_mov_b64_e32 v[6:7], v[248:249]
	v_mov_b64_e32 v[8:9], v[250:251]
	v_mov_b64_e32 v[2:3], v[252:253]
	v_mov_b64_e32 v[4:5], v[254:255]
	v_lshl_add_u64 v[44:45], v[44:45], 0, s[2:3]
	global_load_dwordx4 v[176:179], v[44:45], off offset:-4096
	global_load_dwordx4 v[180:183], v[44:45], off offset:-3072
	global_load_dwordx4 v[184:187], v[44:45], off offset:-2048
	global_load_dwordx4 v[196:199], v[44:45], off offset:-1024
	global_load_dwordx4 v[236:239], v[44:45], off
	global_load_dwordx4 v[240:243], v[44:45], off offset:1024
	global_load_dwordx4 v[248:251], v[44:45], off offset:2048
	global_load_dwordx4 v[252:255], v[44:45], off offset:3072
	v_mov_b32_e32 v78, v31
	v_mov_b32_e32 v79, v23
	v_pk_mul_f32 v[82:83], v[20:21], v[20:21]
	v_pk_mul_f32 v[84:85], v[18:19], v[18:19]
	v_pk_mul_f32 v[86:87], v[12:13], v[12:13]
	v_pk_mul_f32 v[88:89], v[10:11], v[10:11]
	v_mov_b32_e32 v90, v33
	v_mov_b32_e32 v91, v25
	v_mov_b32_e32 v76, v30
	v_mov_b32_e32 v77, v22
	v_mov_b32_e32 v80, v32
	v_mov_b32_e32 v81, v24
	v_pk_mov_b32 v[100:101], v[84:85], v[82:83] op_sel:[1,0]
	v_mov_b32_e32 v85, v83
	v_pk_mov_b32 v[82:83], v[88:89], v[86:87] op_sel:[1,0]
	v_mov_b32_e32 v89, v87
	v_pk_mul_f32 v[78:79], v[78:79], v[78:79]
	v_pk_mul_f32 v[86:87], v[90:91], v[90:91]
	v_pk_fma_f32 v[76:77], v[76:77], v[76:77], v[78:79]
	v_pk_fma_f32 v[78:79], v[80:81], v[80:81], v[86:87]
	v_mul_f32_e32 v92, v27, v27
	v_mul_f32_e32 v94, v29, v29
	v_pk_add_f32 v[80:81], v[100:101], v[84:85]
	v_pk_add_f32 v[76:77], v[76:77], v[78:79]
	v_mul_f32_e32 v102, v14, v14
	v_mul_f32_e32 v103, v15, v15
	v_mul_f32_e32 v104, v16, v16
	v_mul_f32_e32 v105, v17, v17
	v_pk_fma_f32 v[90:91], v[26:27], v[26:27], v[92:93] op_sel_hi:[1,1,0]
	v_pk_fma_f32 v[92:93], v[28:29], v[28:29], v[94:95] op_sel_hi:[1,1,0]
	v_pk_add_f32 v[80:81], v[80:81], v[80:81] op_sel:[0,1] op_sel_hi:[1,0]
	v_pk_add_f32 v[76:77], v[76:77], v[76:77] op_sel:[0,1] op_sel_hi:[1,0]
	v_mov_b32_e32 v91, v104
	v_mov_b32_e32 v93, v105
	v_mov_b32_e32 v81, v103
	v_mov_b32_e32 v77, v102
	v_pk_add_f32 v[78:79], v[90:91], v[92:93]
	v_pk_add_f32 v[76:77], v[76:77], v[80:81]
	v_mul_f32_e32 v96, v7, v7
	v_mul_f32_e32 v98, v9, v9
	v_pk_add_f32 v[82:83], v[82:83], v[88:89]
	v_pk_add_f32 v[76:77], v[76:77], v[78:79]
	v_mul_f32_e32 v106, v2, v2
	v_mul_f32_e32 v107, v3, v3
	v_mul_f32_e32 v108, v4, v4
	v_mul_f32_e32 v109, v5, v5
	v_pk_fma_f32 v[94:95], v[6:7], v[6:7], v[96:97] op_sel_hi:[1,1,0]
	v_pk_fma_f32 v[96:97], v[8:9], v[8:9], v[98:99] op_sel_hi:[1,1,0]
	v_pk_add_f32 v[82:83], v[82:83], v[82:83] op_sel:[0,1] op_sel_hi:[1,0]
	v_pk_add_f32 v[76:77], v[76:77], v[76:77] op_sel:[0,1] op_sel_hi:[1,0]
	v_mov_b32_e32 v95, v108
	v_mov_b32_e32 v97, v109
	v_mov_b32_e32 v83, v107
	v_mov_b32_e32 v77, v106
	v_pk_add_f32 v[84:85], v[94:95], v[96:97]
	v_pk_add_f32 v[76:77], v[76:77], v[82:83]
	v_pk_add_f32 v[76:77], v[76:77], v[84:85]
	v_add_f32_e32 v76, v76, v77
	ds_bpermute_b32 v77, v48, v76
	s_waitcnt lgkmcnt(0)
	v_add_f32_e32 v76, v76, v77
	ds_bpermute_b32 v77, v49, v76
	s_waitcnt lgkmcnt(0)
	v_add_f32_e32 v76, v76, v77
	ds_bpermute_b32 v77, v50, v76
	s_waitcnt lgkmcnt(0)
	v_add_f32_e32 v76, v76, v77
	ds_bpermute_b32 v77, v51, v76
	s_waitcnt lgkmcnt(0)
	v_add_f32_e32 v76, v76, v77
	ds_bpermute_b32 v77, v52, v76
	s_waitcnt lgkmcnt(0)
	v_add_f32_e32 v76, v76, v77
	ds_bpermute_b32 v77, v53, v76
	s_waitcnt lgkmcnt(0)
	v_add_f32_e32 v76, v76, v77
	v_fmamk_f32 v76, v76, 0x3a000000, v54
	v_mul_f32_e32 v77, 0x4f800000, v76
	v_cmp_gt_f32_e32 vcc, s0, v76
	s_nop 1
	v_cndmask_b32_e32 v76, v76, v77, vcc
	v_sqrt_f32_e32 v77, v76
	s_nop 0
	v_add_u32_e32 v78, -1, v77
	v_add_u32_e32 v79, 1, v77
	v_fma_f32 v80, -v78, v77, v76
	v_fma_f32 v81, -v79, v77, v76
	v_cmp_ge_f32_e64 s[4:5], 0, v80
	s_nop 1
	v_cndmask_b32_e64 v77, v77, v78, s[4:5]
	v_cmp_lt_f32_e64 s[4:5], 0, v81
	s_nop 1
	v_cndmask_b32_e64 v77, v77, v79, s[4:5]
	v_mul_f32_e32 v78, 0x37800000, v77
	v_cndmask_b32_e32 v77, v77, v78, vcc
	v_cmp_class_f32_e32 vcc, v76, v55
	s_nop 1
	v_cndmask_b32_e32 v76, v77, v76, vcc
	v_div_scale_f32 v77, s[2:3], v76, v76, 1.0
	v_rcp_f32_e32 v79, v77
	v_div_scale_f32 v78, vcc, 1.0, v76, 1.0
	v_fma_f32 v80, -v77, v79, 1.0
	v_fmac_f32_e32 v79, v80, v79
	v_mul_f32_e32 v80, v78, v79
	v_fma_f32 v81, -v77, v80, v78
	v_fmac_f32_e32 v80, v81, v79
	v_fma_f32 v77, -v77, v80, v78
	v_div_fmas_f32 v77, v77, v79, v80
	v_div_fixup_f32 v76, v77, v76, 1.0
	v_pk_mul_f32 v[30:31], v[30:31], v[76:77] op_sel_hi:[1,0]
	v_pk_mul_f32 v[32:33], v[32:33], v[76:77] op_sel_hi:[1,0]
	v_pk_mul_f32 v[22:23], v[22:23], v[76:77] op_sel_hi:[1,0]
	v_pk_mul_f32 v[24:25], v[24:25], v[76:77] op_sel_hi:[1,0]
	v_pk_mul_f32 v[18:19], v[18:19], v[76:77] op_sel_hi:[1,0]
	v_pk_mul_f32 v[20:21], v[20:21], v[76:77] op_sel_hi:[1,0]
	v_pk_mul_f32 v[26:27], v[26:27], v[76:77] op_sel_hi:[1,0]
	v_pk_mul_f32 v[28:29], v[28:29], v[76:77] op_sel_hi:[1,0]
	v_pk_mul_f32 v[14:15], v[14:15], v[76:77] op_sel_hi:[1,0]
	v_pk_mul_f32 v[16:17], v[16:17], v[76:77] op_sel_hi:[1,0]
	v_pk_mul_f32 v[10:11], v[10:11], v[76:77] op_sel_hi:[1,0]
	v_pk_mul_f32 v[12:13], v[12:13], v[76:77] op_sel_hi:[1,0]
	v_pk_mul_f32 v[6:7], v[6:7], v[76:77] op_sel_hi:[1,0]
	v_pk_mul_f32 v[8:9], v[8:9], v[76:77] op_sel_hi:[1,0]
	v_pk_mul_f32 v[2:3], v[2:3], v[76:77] op_sel_hi:[1,0]
	v_pk_mul_f32 v[4:5], v[4:5], v[76:77] op_sel_hi:[1,0]
	s_waitcnt vmcnt(8)
; __device__ __forceinline__ unsigned pk2(float lo, float hi) { return f2bf(lo) | (f2bf(hi) << 16); }
; __device__ __forceinline__ void xcd_barrier(const XcdBarrier& b) {
;     asm volatile("s_waitcnt vmcnt(0)" ::: "memory");
;     __syncthreads();
;     if (threadIdx.x == 0) {
;         unsigned* bar = b.bar;
;         __builtin_amdgcn_s_waitcnt(0);
;         unsigned nloc = b.st[0], nx = b.st[1];
;         if (nloc == 0u) { xcd_barrier_complete(bar, b.x, nloc, nx); b.st[0] = nloc; b.st[1] = nx; }
; __device__ __forceinline__ void p1_modulate(Frame& F, const Args& A) {
;     ...
;         for (int j = 0; j < 8; ++j) { const int k = 4 * F.lane + 256 * j;
;             const f32x4 g = *(const f32x4*)(A.in[I_N1G] + k), sc = *(const f32x4*)(MOD + b * 12288 + 1 * DM + k), sh = *(const f32x4*)(MOD + b * 12288 + k);
;             const f32x4 u = v[j] * rstd * g * (sc + 1.0f) + sh; if constexpr (NLB > 0) { v2u o; o.x = pk2(u.x, u.y); o.y = pk2(u.z, u.w); *(v2u*)(ur + 256 * j) = o; }
;             int w8 = __builtin_amdgcn_cvt_pk_fp8_f32(u.x, u.y, 0, false); w8 = __builtin_amdgcn_cvt_pk_fp8_f32(u.z, u.w, w8, true); *(int*)(WSP(unsigned char, WS_U8Q) + (size_t)m * DM + 4 * F.lane + 256 * j) = w8; }
	v_mov_b32_e32 v100, 0
	v_pk_mul_f32 v[30:31], v[112:113], v[30:31]
	v_pk_mul_f32 v[32:33], v[114:115], v[32:33]
	v_pk_add_f32 v[64:65], v[144:145], 1.0 op_sel_hi:[1,0]
	v_pk_add_f32 v[66:67], v[146:147], 1.0 op_sel_hi:[1,0]
	v_pk_fma_f32 v[30:31], v[64:65], v[30:31], v[204:205]
	v_pk_fma_f32 v[32:33], v[66:67], v[32:33], v[206:207]
	v_cvt_pk_fp8_f32 v100, v30, v31
	s_nop 0
	v_cvt_pk_fp8_f32 v100, v32, v33 op_sel:[0,0,1]
	global_store_dword v[46:47], v100, off
	v_mov_b32_e32 v101, 0
	v_pk_mul_f32 v[22:23], v[116:117], v[22:23]
	v_pk_mul_f32 v[24:25], v[118:119], v[24:25]
	v_pk_add_f32 v[64:65], v[148:149], 1.0 op_sel_hi:[1,0]
	v_pk_add_f32 v[66:67], v[150:151], 1.0 op_sel_hi:[1,0]
	v_pk_fma_f32 v[22:23], v[64:65], v[22:23], v[208:209]
	v_pk_fma_f32 v[24:25], v[66:67], v[24:25], v[210:211]
	v_cvt_pk_fp8_f32 v101, v22, v23
	s_nop 0
	v_cvt_pk_fp8_f32 v101, v24, v25 op_sel:[0,0,1]
	global_store_dword v[46:47], v101, off offset:256
	v_mov_b32_e32 v102, 0
	v_pk_mul_f32 v[18:19], v[120:121], v[18:19]
	v_pk_mul_f32 v[20:21], v[122:123], v[20:21]
	v_pk_add_f32 v[64:65], v[152:153], 1.0 op_sel_hi:[1,0]
	v_pk_add_f32 v[66:67], v[154:155], 1.0 op_sel_hi:[1,0]
	v_pk_fma_f32 v[18:19], v[64:65], v[18:19], v[212:213]
	v_pk_fma_f32 v[20:21], v[66:67], v[20:21], v[214:215]
	v_cvt_pk_fp8_f32 v102, v18, v19
	s_nop 0
	v_cvt_pk_fp8_f32 v102, v20, v21 op_sel:[0,0,1]
	global_store_dword v[46:47], v102, off offset:512
	v_mov_b32_e32 v103, 0
	v_pk_mul_f32 v[26:27], v[124:125], v[26:27]
	v_pk_mul_f32 v[28:29], v[126:127], v[28:29]
	v_pk_add_f32 v[64:65], v[156:157], 1.0 op_sel_hi:[1,0]
	v_pk_add_f32 v[66:67], v[158:159], 1.0 op_sel_hi:[1,0]
	v_pk_fma_f32 v[26:27], v[64:65], v[26:27], v[216:217]
	v_pk_fma_f32 v[28:29], v[66:67], v[28:29], v[218:219]
	v_cvt_pk_fp8_f32 v103, v26, v27
	s_nop 0
	v_cvt_pk_fp8_f32 v103, v28, v29 op_sel:[0,0,1]
	global_store_dword v[46:47], v103, off offset:768
	v_mov_b32_e32 v104, 0
	v_pk_mul_f32 v[14:15], v[128:129], v[14:15]
	v_pk_mul_f32 v[16:17], v[130:131], v[16:17]
	v_pk_add_f32 v[64:65], v[160:161], 1.0 op_sel_hi:[1,0]
	v_pk_add_f32 v[66:67], v[162:163], 1.0 op_sel_hi:[1,0]
	v_pk_fma_f32 v[14:15], v[64:65], v[14:15], v[220:221]
	v_pk_fma_f32 v[16:17], v[66:67], v[16:17], v[222:223]
	v_cvt_pk_fp8_f32 v104, v14, v15
	s_nop 0
	v_cvt_pk_fp8_f32 v104, v16, v17 op_sel:[0,0,1]
	global_store_dword v[46:47], v104, off offset:1024
	v_mov_b32_e32 v105, 0
	v_pk_mul_f32 v[10:11], v[132:133], v[10:11]
	v_pk_mul_f32 v[12:13], v[134:135], v[12:13]
	v_pk_add_f32 v[64:65], v[164:165], 1.0 op_sel_hi:[1,0]
	v_pk_add_f32 v[66:67], v[166:167], 1.0 op_sel_hi:[1,0]
	v_pk_fma_f32 v[10:11], v[64:65], v[10:11], v[224:225]
	v_pk_fma_f32 v[12:13], v[66:67], v[12:13], v[226:227]
	v_cvt_pk_fp8_f32 v105, v10, v11
	s_nop 0
	v_cvt_pk_fp8_f32 v105, v12, v13 op_sel:[0,0,1]
	global_store_dword v[46:47], v105, off offset:1280
	v_mov_b32_e32 v106, 0
	v_pk_mul_f32 v[6:7], v[136:137], v[6:7]
	v_pk_mul_f32 v[8:9], v[138:139], v[8:9]
	v_pk_add_f32 v[64:65], v[168:169], 1.0 op_sel_hi:[1,0]
	v_pk_add_f32 v[66:67], v[170:171], 1.0 op_sel_hi:[1,0]
	v_pk_fma_f32 v[6:7], v[64:65], v[6:7], v[228:229]
	v_pk_fma_f32 v[8:9], v[66:67], v[8:9], v[230:231]
	v_cvt_pk_fp8_f32 v106, v6, v7
	s_nop 0
	v_cvt_pk_fp8_f32 v106, v8, v9 op_sel:[0,0,1]
	global_store_dword v[46:47], v106, off offset:1536
	v_mov_b32_e32 v107, 0
	v_pk_mul_f32 v[2:3], v[140:141], v[2:3]
	v_pk_mul_f32 v[4:5], v[142:143], v[4:5]
	v_pk_add_f32 v[64:65], v[172:173], 1.0 op_sel_hi:[1,0]
	v_pk_add_f32 v[66:67], v[174:175], 1.0 op_sel_hi:[1,0]
	v_pk_fma_f32 v[2:3], v[64:65], v[2:3], v[232:233]
	v_pk_fma_f32 v[4:5], v[66:67], v[4:5], v[234:235]
	v_cvt_pk_fp8_f32 v107, v2, v3
	s_nop 0
	v_cvt_pk_fp8_f32 v107, v4, v5 op_sel:[0,0,1]
	global_store_dword v[46:47], v107, off offset:1792
	v_lshl_add_u64 v[46:47], v[46:47], 0, s[54:55]
	s_cbranch_scc1 .LBB0_55
.LBB0_56:
	s_waitcnt vmcnt(0)
	s_cmp_gt_i32 s93, 2
	s_cselect_b64 s[4:5], -1, 0
	s_and_b64 s[0:1], s[6:7], s[4:5]
	v_writelane_b32 v246, s86, 41
	s_andn2_b64 vcc, exec, s[0:1]
	v_writelane_b32 v246, s90, 42
	v_writelane_b32 v246, s91, 43
	s_cbranch_vccnz .LBB0_111
	s_waitcnt vmcnt(0)
	s_waitcnt lgkmcnt(0)
	s_barrier
	s_mov_b64 s[6:7], exec
	v_readlane_b32 s0, v246, 38
	v_readlane_b32 s1, v246, 39
	s_and_b64 s[0:1], s[6:7], s[0:1]
	s_mov_b64 exec, s[0:1]
	s_cbranch_execz .LBB0_110
	s_add_i32 s0, 0, 0x27160
	v_mov_b32_e32 v2, s0
	s_waitcnt vmcnt(0) expcnt(0) lgkmcnt(0)
	ds_read_b32 v4, v2
	s_add_i32 s0, 0, 0x27164
	v_mov_b32_e32 v2, s0
	ds_read_b32 v2, v2
	s_waitcnt lgkmcnt(1)
	v_cmp_ne_u32_e32 vcc, 0, v4
	s_cbranch_vccnz .LBB0_74
	s_add_u32 s8, s30, 0x4200
	s_addc_u32 s9, s31, 0
	s_add_u32 s42, s30, 0x4400
	s_addc_u32 s43, s31, 0
	s_add_u32 s44, s30, 0x4500
	s_addc_u32 s45, s31, 0
	s_add_u32 s46, s30, 0x4600
	s_addc_u32 s47, s31, 0
	s_add_u32 s54, s30, 0x4700
	s_addc_u32 s55, s31, 0
	s_add_u32 s56, s30, 0x4800
	s_addc_u32 s57, s31, 0
	s_add_u32 s58, s30, 0x4900
	s_addc_u32 s59, s31, 0
	s_add_u32 s60, s30, 0x4a00
	s_addc_u32 s61, s31, 0
	s_add_u32 s62, s30, 0x4b00
	s_addc_u32 s63, s31, 0
	s_add_u32 s70, s30, 0x4c00
	s_addc_u32 s71, s31, 0
	s_add_u32 s72, s30, 0x4d00
	s_addc_u32 s73, s31, 0
	s_add_u32 s74, s30, 0x4e00
	s_addc_u32 s75, s31, 0
	s_add_u32 s76, s30, 0x4f00
	v_readlane_b32 s2, v246, 1
	s_addc_u32 s77, s31, 0
	v_readlane_b32 s3, v246, 2
	s_add_u32 s78, s30, 0x5000
	s_load_dwordx2 s[0:1], s[2:3], 0x4
	s_addc_u32 s79, s31, 0
	s_add_u32 s80, s30, 0x5100
	s_addc_u32 s81, s31, 0
	s_add_u32 s82, s30, 0x5200
	s_addc_u32 s83, s31, 0
	s_waitcnt lgkmcnt(0)
	s_mul_i32 s0, s0, s86
	s_add_u32 s84, s30, 0x5300
	s_mul_i32 s0, s0, s1
	s_addc_u32 s85, s31, 0
	s_mov_b32 s1, 1
	v_mov_b32_e32 v18, 0
	s_branch .LBB0_62
